# Final combine phase: row loads (read once) and output stores (never re-read) carry the nt hint
# speedup vs baseline: 1.0126x; 1.0008x over previous
; __global__ void __launch_bounds__(NWAVES * 64, 2) trunk_fwd(Args args) {
;     ...
;                 for (int m = gw; m < M; m += ngw) {
;                     const int p0 = TOKP[2 * m], p1 = TOKP[2 * m + 1]; const float g0 = TOKW[2 * m], g1 = TOKW[2 * m + 1];
;                     const f32x4* xr = (const f32x4*)(XA + (size_t)m * D) + lane; const v2u* y0 = (const v2u*)(YPERM + (size_t)p0 * D) + lane; const v2u* y1 = (const v2u*)(YPERM + (size_t)p1 * D) + lane;
;                     const v2u* z0 = (const v2u*)(HPERM + (size_t)p0 * D) + lane; const v2u* z1 = (const v2u*)(HPERM + (size_t)p1 * D) + lane;
;                     f32x4 v[8]; float s = 0.f;
; #pragma unroll
;                     for (int jj = 0; jj < 8; ++jj) { const v2u a = y0[64 * jj], c = y1[64 * jj], a2 = z0[64 * jj], c2 = z1[64 * jj]; f32x4 x = xr[64 * jj];
;                         x.x += g0 * (bflo(a.x) + bflo(a2.x)) + g1 * (bflo(c.x) + bflo(c2.x)); x.y += g0 * (bfhi(a.x) + bfhi(a2.x)) + g1 * (bfhi(c.x) + bfhi(c2.x));
;                         x.z += g0 * (bflo(a.y) + bflo(a2.y)) + g1 * (bflo(c.y) + bflo(c2.y)); x.w += g0 * (bfhi(a.y) + bfhi(a2.y)) + g1 * (bfhi(c.y) + bfhi(c2.y));
;                         v[jj] = x; s += (x.x * x.x + x.y * x.y) + (x.z * x.z + x.w * x.w); }
;                     const float rstd = 1.0f / sqrtf(wave_sum(s) * (1.0f / D) + EPS);
.LBB0_1349:
	s_ashr_i32 s11, s10, 31
	s_lshl_b64 s[4:5], s[10:11], 2
	s_add_u32 s14, s18, s4
	s_addc_u32 s15, s19, s5
	global_load_dwordx2 v[2:3], v187, s[14:15]
	s_add_i32 s14, s10, 1
	s_ashr_i32 s15, s14, 31
	s_add_u32 s4, s23, s4
	s_addc_u32 s5, s17, s5
	global_load_dword v52, v187, s[4:5]
	s_lshl_b64 s[4:5], s[14:15], 2
	s_add_u32 s4, s23, s4
	s_addc_u32 s5, s17, s5
	global_load_dword v53, v187, s[4:5]
	v_lshl_add_u64 v[4:5], s[12:13], 0, v[186:187]
	s_mov_b32 s4, 0x36da1000
	s_add_i32 s7, s7, s16
	s_waitcnt vmcnt(0)
	v_ashrrev_i32_e32 v7, 31, v2
	v_mov_b32_e32 v6, v2
	v_lshlrev_b64 v[6:7], 12, v[6:7]
	v_lshl_add_u64 v[18:19], v[28:29], 0, v[6:7]
	v_lshl_add_u64 v[76:77], v[30:31], 0, v[6:7]
	v_add_co_u32_e32 v6, vcc, s4, v4
	v_ashrrev_i32_e32 v9, 31, v3
	s_nop 0
	v_addc_co_u32_e32 v7, vcc, 0, v5, vcc
	v_mov_b32_e32 v8, v3
	v_add_co_u32_e32 v96, vcc, s28, v4
	v_lshlrev_b64 v[2:3], 12, v[8:9]
	s_nop 0
	v_addc_co_u32_e32 v97, vcc, 0, v5, vcc
	v_lshl_add_u64 v[68:69], v[28:29], 0, v[2:3]
	v_lshl_add_u64 v[92:93], v[30:31], 0, v[2:3]
	global_load_dwordx2 v[122:123], v[18:19], off nt
	global_load_dwordx2 v[156:157], v[68:69], off nt
	global_load_dwordx2 v[158:159], v[76:77], off nt
	global_load_dwordx2 v[160:161], v[92:93], off nt
	global_load_dwordx4 v[162:165], v[96:97], off offset:-4096 nt
	global_load_dwordx2 v[166:167], v[18:19], off offset:512 nt
	global_load_dwordx2 v[168:169], v[68:69], off offset:512 nt
	global_load_dwordx2 v[170:171], v[76:77], off offset:512 nt
	global_load_dwordx2 v[172:173], v[92:93], off offset:512 nt
	global_load_dwordx4 v[174:177], v[6:7], off offset:1024 nt
	global_load_dwordx2 v[178:179], v[18:19], off offset:1024 nt
	global_load_dwordx2 v[180:181], v[68:69], off offset:1024 nt
	global_load_dwordx2 v[182:183], v[76:77], off offset:1024 nt
	global_load_dwordx2 v[184:185], v[92:93], off offset:1024 nt
	global_load_dwordx4 v[200:203], v[6:7], off offset:2048 nt
	global_load_dwordx2 v[204:205], v[18:19], off offset:1536 nt
	global_load_dwordx2 v[206:207], v[68:69], off offset:1536 nt
	global_load_dwordx2 v[208:209], v[76:77], off offset:1536 nt
	global_load_dwordx2 v[210:211], v[92:93], off offset:1536 nt
	global_load_dwordx4 v[212:215], v[6:7], off offset:3072 nt
	global_load_dwordx2 v[216:217], v[18:19], off offset:2048 nt
	global_load_dwordx2 v[218:219], v[68:69], off offset:2048 nt
	global_load_dwordx2 v[220:221], v[76:77], off offset:2048 nt
	global_load_dwordx2 v[222:223], v[92:93], off offset:2048 nt
	global_load_dwordx4 v[232:235], v[96:97], off nt
	global_load_dwordx2 v[236:237], v[18:19], off offset:2560 nt
	global_load_dwordx2 v[238:239], v[68:69], off offset:2560 nt
	global_load_dwordx2 v[240:241], v[76:77], off offset:2560 nt
	global_load_dwordx2 v[242:243], v[92:93], off offset:2560 nt
	global_load_dwordx4 v[244:247], v[96:97], off offset:1024 nt
	v_mov_b32_e32 v94, v53
	s_waitcnt vmcnt(24)
	v_lshlrev_b32_e32 v16, 16, v166
	s_waitcnt vmcnt(23)
	v_lshlrev_b32_e32 v17, 16, v168
	s_waitcnt vmcnt(22)
	v_lshlrev_b32_e32 v20, 16, v170
	s_waitcnt vmcnt(21)
	v_lshlrev_b32_e32 v21, 16, v172
	v_pk_add_f32 v[16:17], v[16:17], v[20:21]
	v_and_b32_e32 v21, 0xffff0000, v172
	v_pk_mul_f32 v[64:65], v[52:53], v[16:17]
	v_and_b32_e32 v17, 0xffff0000, v168
	v_and_b32_e32 v16, 0xffff0000, v166
	v_and_b32_e32 v20, 0xffff0000, v170
	v_pk_add_f32 v[16:17], v[16:17], v[20:21]
	v_lshlrev_b32_e32 v21, 16, v173
	v_pk_mul_f32 v[66:67], v[52:53], v[16:17]
	v_lshlrev_b32_e32 v17, 16, v169
	v_lshlrev_b32_e32 v16, 16, v167
	v_lshlrev_b32_e32 v20, 16, v171
	v_and_b32_e32 v169, 0xffff0000, v169
	v_and_b32_e32 v168, 0xffff0000, v167
	v_and_b32_e32 v167, 0xffff0000, v173
	v_and_b32_e32 v166, 0xffff0000, v171
	v_pk_add_f32 v[16:17], v[16:17], v[20:21]
	v_pk_add_f32 v[2:3], v[168:169], v[166:167]
	v_pk_mul_f32 v[54:55], v[52:53], v[16:17]
	v_pk_mul_f32 v[56:57], v[52:53], v[2:3]
	v_lshlrev_b32_e32 v120, 16, v160
	v_and_b32_e32 v121, 0xffff0000, v160
	v_lshlrev_b32_e32 v160, 16, v161
	v_and_b32_e32 v161, 0xffff0000, v161
	s_waitcnt vmcnt(19)
	v_lshlrev_b32_e32 v23, 16, v179
	v_lshlrev_b32_e32 v22, 16, v178
	s_waitcnt vmcnt(17)
	v_lshlrev_b32_e32 v43, 16, v183
	v_lshlrev_b32_e32 v42, 16, v182
	v_and_b32_e32 v179, 0xffff0000, v179
	v_and_b32_e32 v178, 0xffff0000, v178
	v_and_b32_e32 v183, 0xffff0000, v183
	v_and_b32_e32 v182, 0xffff0000, v182
	v_pk_add_f32 v[22:23], v[22:23], v[42:43]
	v_lshlrev_b32_e32 v43, 16, v181
	v_lshlrev_b32_e32 v42, 16, v180
	s_waitcnt vmcnt(16)
	v_lshlrev_b32_e32 v45, 16, v185
	v_lshlrev_b32_e32 v44, 16, v184
	v_pk_add_f32 v[8:9], v[178:179], v[182:183]
	v_and_b32_e32 v181, 0xffff0000, v181
	v_and_b32_e32 v180, 0xffff0000, v180
	v_and_b32_e32 v183, 0xffff0000, v185
	v_and_b32_e32 v182, 0xffff0000, v184
	v_pk_add_f32 v[42:43], v[42:43], v[44:45]
	v_pk_add_f32 v[14:15], v[180:181], v[182:183]
	v_pk_mul_f32 v[42:43], v[94:95], v[42:43] op_sel_hi:[0,1]
	v_pk_mul_f32 v[14:15], v[94:95], v[14:15] op_sel_hi:[0,1]
	v_pk_fma_f32 v[22:23], v[52:53], v[22:23], v[42:43] op_sel_hi:[0,1,1]
	s_waitcnt vmcnt(15)
	v_mov_b32_e32 v42, v200
	v_mov_b32_e32 v43, v202
	v_pk_fma_f32 v[8:9], v[52:53], v[8:9], v[14:15] op_sel_hi:[0,1,1]
	v_mov_b32_e32 v202, v201
	v_pk_add_f32 v[58:59], v[42:43], v[22:23]
	v_pk_add_f32 v[42:43], v[202:203], v[8:9]
	global_load_dwordx2 v[178:179], v[18:19], off offset:3072 nt
	global_load_dwordx2 v[180:181], v[68:69], off offset:3072 nt
	global_load_dwordx2 v[182:183], v[76:77], off offset:3072 nt
	global_load_dwordx2 v[184:185], v[92:93], off offset:3072 nt
	global_load_dwordx4 v[200:203], v[96:97], off offset:2048 nt
	s_nop 0
	v_pk_mul_f32 v[2:3], v[42:43], v[42:43]
	s_nop 0
	v_pk_fma_f32 v[2:3], v[58:59], v[58:59], v[2:3]
	s_nop 0
	v_pk_add_f32 v[62:63], v[2:3], v[2:3] op_sel:[0,1] op_sel_hi:[1,0]
	s_waitcnt vmcnt(19)
; __global__ void __launch_bounds__(NWAVES * 64, 2) trunk_fwd(Args args) {
;     ...
; #pragma unroll
;                     for (int jj = 0; jj < 8; ++jj) { const v2u a = y0[64 * jj], c = y1[64 * jj], a2 = z0[64 * jj], c2 = z1[64 * jj]; f32x4 x = xr[64 * jj];
;                         x.x += g0 * (bflo(a.x) + bflo(a2.x)) + g1 * (bflo(c.x) + bflo(c2.x)); x.y += g0 * (bfhi(a.x) + bfhi(a2.x)) + g1 * (bfhi(c.x) + bfhi(c2.x));
;                         x.z += g0 * (bflo(a.y) + bflo(a2.y)) + g1 * (bflo(c.y) + bflo(c2.y)); x.w += g0 * (bfhi(a.y) + bfhi(a2.y)) + g1 * (bfhi(c.y) + bfhi(c2.y));
;                         v[jj] = x; s += (x.x * x.x + x.y * x.y) + (x.z * x.z + x.w * x.w); }
;                     const float rstd = 1.0f / sqrtf(wave_sum(s) * (1.0f / D) + EPS);
	v_lshlrev_b32_e32 v6, 16, v204
	v_and_b32_e32 v7, 0xffff0000, v204
	s_waitcnt vmcnt(17)
	v_lshlrev_b32_e32 v22, 16, v208
	v_and_b32_e32 v23, 0xffff0000, v208
	v_pk_add_f32 v[6:7], v[6:7], v[22:23]
	v_lshlrev_b32_e32 v22, 16, v206
	v_and_b32_e32 v23, 0xffff0000, v206
	s_waitcnt vmcnt(16)
	v_lshlrev_b32_e32 v44, 16, v210
	v_and_b32_e32 v45, 0xffff0000, v210
	v_pk_add_f32 v[22:23], v[22:23], v[44:45]
	v_lshlrev_b32_e32 v204, 16, v211
	v_pk_mul_f32 v[22:23], v[94:95], v[22:23] op_sel_hi:[0,1]
	v_pk_fma_f32 v[6:7], v[52:53], v[6:7], v[22:23] op_sel_hi:[0,1,1]
	s_waitcnt vmcnt(15)
	v_pk_add_f32 v[44:45], v[212:213], v[6:7]
	v_lshlrev_b32_e32 v6, 16, v209
	v_mul_f32_e32 v212, v45, v45
	v_pk_fma_f32 v[82:83], v[44:45], v[44:45], v[212:213] op_sel_hi:[1,1,0]
	v_lshlrev_b32_e32 v212, 16, v205
	v_and_b32_e32 v213, 0xffff0000, v205
	v_and_b32_e32 v7, 0xffff0000, v209
	v_pk_add_f32 v[2:3], v[212:213], v[6:7]
	v_lshlrev_b32_e32 v6, 16, v207
	v_and_b32_e32 v7, 0xffff0000, v207
	v_and_b32_e32 v205, 0xffff0000, v211
	v_pk_add_f32 v[6:7], v[6:7], v[204:205]
	s_nop 0
	v_pk_mul_f32 v[6:7], v[94:95], v[6:7] op_sel_hi:[0,1]
	v_pk_fma_f32 v[2:3], v[52:53], v[2:3], v[6:7] op_sel_hi:[0,1,1]
	v_pk_add_f32 v[46:47], v[214:215], v[2:3]
	global_load_dwordx2 v[166:167], v[18:19], off offset:3584 nt
	global_load_dwordx2 v[168:169], v[68:69], off offset:3584 nt
	global_load_dwordx2 v[170:171], v[76:77], off offset:3584 nt
	global_load_dwordx2 v[172:173], v[92:93], off offset:3584 nt
	global_load_dwordx4 v[212:215], v[96:97], off offset:3072 nt
	s_nop 0
	v_mul_f32_e32 v2, v47, v47
	v_pk_fma_f32 v[86:87], v[46:47], v[46:47], v[2:3] op_sel_hi:[1,1,0]
	s_waitcnt vmcnt(19)
	v_lshlrev_b32_e32 v206, 16, v217
	s_waitcnt vmcnt(18)
	v_lshlrev_b32_e32 v207, 16, v219
	s_waitcnt vmcnt(17)
	v_lshlrev_b32_e32 v208, 16, v221
	s_waitcnt vmcnt(16)
	v_lshlrev_b32_e32 v209, 16, v223
	v_pk_add_f32 v[78:79], v[206:207], v[208:209]
	v_and_b32_e32 v207, 0xffff0000, v219
	v_and_b32_e32 v206, 0xffff0000, v217
	v_and_b32_e32 v209, 0xffff0000, v223
	v_and_b32_e32 v208, 0xffff0000, v221
	v_pk_add_f32 v[88:89], v[206:207], v[208:209]
	v_lshlrev_b32_e32 v206, 16, v216
	v_and_b32_e32 v207, 0xffff0000, v216
	v_lshlrev_b32_e32 v216, 16, v220
	v_and_b32_e32 v217, 0xffff0000, v220
	v_lshlrev_b32_e32 v220, 16, v218
	v_and_b32_e32 v221, 0xffff0000, v218
	v_lshlrev_b32_e32 v218, 16, v222
	v_and_b32_e32 v219, 0xffff0000, v222
	v_pk_add_f32 v[4:5], v[220:221], v[218:219]
	v_pk_add_f32 v[2:3], v[206:207], v[216:217]
	v_pk_mul_f32 v[4:5], v[94:95], v[4:5] op_sel_hi:[0,1]
	v_pk_fma_f32 v[2:3], v[52:53], v[2:3], v[4:5] op_sel_hi:[0,1,1]
	s_waitcnt vmcnt(15)
	v_pk_add_f32 v[48:49], v[232:233], v[2:3]
	s_nop 0
	v_mul_f32_e32 v2, v49, v49
	v_pk_fma_f32 v[90:91], v[48:49], v[48:49], v[2:3] op_sel_hi:[1,1,0]
	s_waitcnt vmcnt(14)
	v_lshlrev_b32_e32 v232, 16, v236
	s_waitcnt vmcnt(13)
	v_lshlrev_b32_e32 v233, 16, v238
	s_waitcnt vmcnt(12)
	v_lshlrev_b32_e32 v50, 16, v240
	s_waitcnt vmcnt(11)
	v_lshlrev_b32_e32 v51, 16, v242
	v_pk_add_f32 v[20:21], v[232:233], v[50:51]
	v_and_b32_e32 v240, 0xffff0000, v240
	v_pk_mul_f32 v[20:21], v[52:53], v[20:21]
	v_and_b32_e32 v236, 0xffff0000, v236
	v_add_f32_e32 v20, v20, v21
	v_add_f32_e32 v236, v240, v236
	s_waitcnt vmcnt(10)
	v_add_f32_e32 v244, v244, v20
	v_mul_f32_e32 v20, v52, v236
	v_and_b32_e32 v236, 0xffff0000, v242
	v_and_b32_e32 v238, 0xffff0000, v238
	v_add_f32_e32 v236, v236, v238
	v_mul_f32_e32 v114, v53, v236
	v_lshlrev_b32_e32 v51, 16, v239
	v_lshlrev_b32_e32 v50, 16, v237
	v_lshlrev_b32_e32 v61, 16, v243
	v_lshlrev_b32_e32 v60, 16, v241
	v_and_b32_e32 v239, 0xffff0000, v239
	v_and_b32_e32 v238, 0xffff0000, v237
	v_and_b32_e32 v237, 0xffff0000, v243
	v_and_b32_e32 v236, 0xffff0000, v241
	v_pk_add_f32 v[50:51], v[50:51], v[60:61]
	v_pk_add_f32 v[2:3], v[238:239], v[236:237]
	v_pk_mul_f32 v[60:61], v[52:53], v[50:51]
	v_pk_mul_f32 v[50:51], v[52:53], v[2:3]
	v_mul_f32_e32 v80, v244, v244
	s_waitcnt vmcnt(9)
	v_lshlrev_b32_e32 v70, 16, v178
	s_waitcnt vmcnt(8)
	v_lshlrev_b32_e32 v71, 16, v180
	s_waitcnt vmcnt(7)
	v_lshlrev_b32_e32 v84, 16, v182
	s_waitcnt vmcnt(6)
	v_lshlrev_b32_e32 v85, 16, v184
	v_pk_add_f32 v[84:85], v[70:71], v[84:85]
	v_and_b32_e32 v71, 0xffff0000, v180
	v_and_b32_e32 v70, 0xffff0000, v178
	v_and_b32_e32 v117, 0xffff0000, v184
	v_and_b32_e32 v116, 0xffff0000, v182
	v_pk_add_f32 v[70:71], v[70:71], v[116:117]
	v_and_b32_e32 v180, 0xffff0000, v179
	v_pk_mul_f32 v[70:71], v[52:53], v[70:71]
	v_lshlrev_b32_e32 v117, 16, v185
	v_add_f32_e32 v178, v70, v71
	s_waitcnt vmcnt(5)
	v_add_f32_e32 v184, v201, v178
	v_lshlrev_b32_e32 v71, 16, v181
	v_lshlrev_b32_e32 v70, 16, v179
	v_and_b32_e32 v181, 0xffff0000, v181
	v_and_b32_e32 v179, 0xffff0000, v185
	v_and_b32_e32 v178, 0xffff0000, v183
	v_pk_add_f32 v[2:3], v[180:181], v[178:179]
	v_lshlrev_b32_e32 v116, 16, v183
	v_pk_mul_f32 v[2:3], v[52:53], v[2:3]
	v_pk_add_f32 v[70:71], v[70:71], v[116:117]
	v_add_f32_e32 v2, v2, v3
	v_add_f32_e32 v185, v203, v2
	s_nop 0
	s_nop 0
	s_nop 0
	v_mov_b32_e32 v92, v245
	v_mov_b32_e32 v182, v234
	v_mul_f32_e32 v234, v53, v79
	v_pk_fma_f32 v[78:79], v[52:53], v[78:79], v[234:235] op_sel_hi:[1,1,0]
	v_mul_f32_e32 v234, v53, v89
	v_mov_b32_e32 v93, v52
	v_mul_f32_e32 v74, v184, v184
	v_mul_f32_e32 v72, v185, v185
	s_waitcnt vmcnt(4)
	v_and_b32_e32 v21, 0xffff0000, v166
	s_waitcnt vmcnt(3)
	v_and_b32_e32 v201, 0xffff0000, v168
	s_waitcnt vmcnt(2)
	v_and_b32_e32 v115, 0xffff0000, v170
	s_waitcnt vmcnt(1)
; __global__ void __launch_bounds__(NWAVES * 64, 2) trunk_fwd(Args args) {
;     ...
;                 for (int m = gw; m < M; m += ngw) {
;                     const int p0 = TOKP[2 * m], p1 = TOKP[2 * m + 1]; const float g0 = TOKW[2 * m], g1 = TOKW[2 * m + 1];
;                     const f32x4* xr = (const f32x4*)(XA + (size_t)m * D) + lane; const v2u* y0 = (const v2u*)(YPERM + (size_t)p0 * D) + lane; const v2u* y1 = (const v2u*)(YPERM + (size_t)p1 * D) + lane;
;                     const v2u* z0 = (const v2u*)(HPERM + (size_t)p0 * D) + lane; const v2u* z1 = (const v2u*)(HPERM + (size_t)p1 * D) + lane;
;                     f32x4 v[8]; float s = 0.f;
; #pragma unroll
;                     for (int jj = 0; jj < 8; ++jj) { const v2u a = y0[64 * jj], c = y1[64 * jj], a2 = z0[64 * jj], c2 = z1[64 * jj]; f32x4 x = xr[64 * jj];
;                         x.x += g0 * (bflo(a.x) + bflo(a2.x)) + g1 * (bflo(c.x) + bflo(c2.x)); x.y += g0 * (bfhi(a.x) + bfhi(a2.x)) + g1 * (bfhi(c.x) + bfhi(c2.x));
;                         x.z += g0 * (bflo(a.y) + bflo(a2.y)) + g1 * (bflo(c.y) + bflo(c2.y)); x.w += g0 * (bfhi(a.y) + bfhi(a2.y)) + g1 * (bfhi(c.y) + bfhi(c2.y));
;                         v[jj] = x; s += (x.x * x.x + x.y * x.y) + (x.z * x.z + x.w * x.w); }
;                     const float rstd = 1.0f / sqrtf(wave_sum(s) * (1.0f / D) + EPS);
	v_and_b32_e32 v245, 0xffff0000, v172
	v_add_f32_e32 v245, v245, v201
	v_mul_f32_e32 v97, v53, v245
	v_lshlrev_b32_e32 v245, 16, v167
	v_lshlrev_b32_e32 v201, 16, v171
	v_add_f32_e32 v245, v201, v245
	v_mul_f32_e32 v201, v52, v245
	v_lshlrev_b32_e32 v245, 16, v169
	v_lshlrev_b32_e32 v203, 16, v173
	v_add_f32_e32 v245, v203, v245
	v_pk_add_f32 v[20:21], v[20:21], v[114:115]
	v_mul_f32_e32 v114, v53, v245
	v_and_b32_e32 v245, 0xffff0000, v171
	v_and_b32_e32 v203, 0xffff0000, v167
	v_add_f32_e32 v245, v245, v203
	v_lshlrev_b32_e32 v183, 16, v166
	v_lshlrev_b32_e32 v95, 16, v168
	v_lshlrev_b32_e32 v81, 16, v172
	v_mul_f32_e32 v203, v52, v245
	v_and_b32_e32 v245, 0xffff0000, v173
	v_and_b32_e32 v166, 0xffff0000, v169
	v_lshlrev_b32_e32 v168, 16, v122
	v_and_b32_e32 v169, 0xffff0000, v122
	v_lshlrev_b32_e32 v172, 16, v158
	v_and_b32_e32 v173, 0xffff0000, v158
	v_pk_add_f32 v[116:117], v[168:169], v[172:173]
	v_lshlrev_b32_e32 v172, 16, v156
	v_and_b32_e32 v173, 0xffff0000, v156
	v_lshlrev_b32_e32 v156, 16, v157
	v_and_b32_e32 v157, 0xffff0000, v157
	v_pk_add_f32 v[118:119], v[172:173], v[120:121]
	v_pk_add_f32 v[100:101], v[156:157], v[160:161]
	v_lshlrev_b32_e32 v83, 16, v170
	v_pk_mul_f32 v[118:119], v[94:95], v[118:119] op_sel_hi:[0,1]
	v_pk_mul_f32 v[100:101], v[94:95], v[100:101] op_sel_hi:[0,1]
	v_mov_b32_e32 v94, v235
	v_pk_fma_f32 v[22:23], v[52:53], v[88:89], v[234:235] op_sel_hi:[1,1,0]
	v_lshlrev_b32_e32 v122, 16, v123
	v_and_b32_e32 v123, 0xffff0000, v123
	v_lshlrev_b32_e32 v158, 16, v159
	v_and_b32_e32 v159, 0xffff0000, v159
	v_mov_b32_e32 v79, v83
	v_mov_b32_e32 v23, v81
	v_pk_add_f32 v[104:105], v[122:123], v[158:159]
	v_pk_add_f32 v[78:79], v[182:183], v[78:79]
	v_pk_add_f32 v[88:89], v[94:95], v[22:23]
	v_pk_fma_f32 v[100:101], v[52:53], v[104:105], v[100:101] op_sel_hi:[0,1,1]
	v_mov_b32_e32 v182, v78
	v_mov_b32_e32 v183, v52
	v_mov_b32_e32 v22, v88
	v_mov_b32_e32 v23, v53
	v_pk_add_f32 v[68:69], v[92:93], v[20:21]
	v_pk_mul_f32 v[92:93], v[92:93], v[20:21]
	v_pk_add_f32 v[26:27], v[164:165], v[100:101]
	v_pk_mul_f32 v[100:101], v[182:183], v[78:79]
	v_pk_mul_f32 v[22:23], v[22:23], v[88:89]
	v_mov_b32_e32 v92, v68
	v_mov_b32_e32 v83, v101
	v_mov_b32_e32 v87, v23
	v_pk_fma_f32 v[22:23], v[182:183], v[78:79], v[22:23]
	s_waitcnt vmcnt(0)
	v_mov_b32_e32 v91, v212
	v_mov_b32_e32 v96, v68
	v_pk_add_f32 v[86:87], v[82:83], v[86:87]
	v_pk_add_f32 v[90:91], v[90:91], v[22:23]
	v_pk_mul_f32 v[22:23], v[68:69], v[68:69]
	v_pk_add_f32 v[82:83], v[92:93], v[96:97]
	v_mov_b32_e32 v81, v213
	v_mov_b32_e32 v23, v83
	v_pk_add_f32 v[22:23], v[80:81], v[22:23]
	v_mul_f32_e32 v80, v53, v85
	v_pk_fma_f32 v[80:81], v[52:53], v[84:85], v[80:81] op_sel_hi:[1,1,0]
	v_add_f32_e32 v245, v245, v166
	v_mov_b32_e32 v81, v114
	v_pk_add_f32 v[14:15], v[200:201], v[80:81]
	v_mov_b32_e32 v81, v214
	v_mul_f32_e32 v214, v53, v71
	v_mul_f32_e32 v245, v53, v245
	v_pk_fma_f32 v[116:117], v[52:53], v[116:117], v[118:119] op_sel_hi:[0,1,1]
	v_pk_fma_f32 v[52:53], v[52:53], v[70:71], v[214:215] op_sel_hi:[1,1,0]
	v_mov_b32_e32 v80, v14
	v_mov_b32_e32 v53, v245
	v_pk_add_f32 v[16:17], v[202:203], v[52:53]
	v_pk_add_f32 v[80:81], v[80:81], v[14:15]
	v_mov_b32_e32 v214, v16
	v_pk_add_f32 v[4:5], v[214:215], v[16:17]
	v_pk_fma_f32 v[52:53], v[14:15], v[14:15], v[74:75]
	v_pk_mul_f32 v[70:71], v[80:81], v[80:81]
	v_pk_mul_f32 v[84:85], v[4:5], v[4:5]
	v_mov_b32_e32 v53, v71
	v_pk_fma_f32 v[70:71], v[16:17], v[16:17], v[72:73]
	v_pk_add_f32 v[24:25], v[162:163], v[116:117]
	v_mov_b32_e32 v71, v85
	v_pk_add_f32 v[70:71], v[52:53], v[70:71]
	v_mov_b32_e32 v52, v64
	v_mov_b32_e32 v53, v66
	v_mov_b32_e32 v66, v65
	v_pk_add_f32 v[52:53], v[52:53], v[66:67]
	v_mov_b32_e32 v64, v25
	v_pk_add_f32 v[52:53], v[174:175], v[52:53]
	v_mov_b32_e32 v174, v24
	v_mov_b32_e32 v65, v53
	v_mov_b32_e32 v175, v52
	v_pk_mul_f32 v[64:65], v[64:65], v[64:65]
	v_pk_fma_f32 v[10:11], v[174:175], v[174:175], v[64:65]
	v_mov_b32_e32 v64, v54
	v_mov_b32_e32 v65, v56
	v_mov_b32_e32 v56, v55
	v_pk_add_f32 v[54:55], v[64:65], v[56:57]
	v_mov_b32_e32 v56, v27
	v_pk_add_f32 v[54:55], v[176:177], v[54:55]
	v_mov_b32_e32 v176, v26
	v_mov_b32_e32 v57, v55
	v_mov_b32_e32 v177, v54
	v_pk_mul_f32 v[56:57], v[56:57], v[56:57]
	v_lshl_add_u64 v[76:77], s[8:9], 0, v[186:187]
	v_pk_fma_f32 v[12:13], v[176:177], v[176:177], v[56:57]
	v_mov_b32_e32 v79, v88
	v_pk_add_f32 v[10:11], v[10:11], v[12:13]
	v_mov_b32_e32 v245, v68
	v_pk_add_f32 v[10:11], v[10:11], v[10:11] op_sel:[0,1] op_sel_hi:[1,0]
	s_add_u32 s8, s8, s38
	v_pk_add_f32 v[10:11], v[10:11], v[62:63]
	s_addc_u32 s9, s9, s39
	v_mov_b32_e32 v11, v212
	v_pk_add_f32 v[10:11], v[10:11], v[86:87]
	s_add_i32 s10, s10, s21
	v_pk_add_f32 v[56:57], v[10:11], v[90:91]
	v_pk_mul_f32 v[12:13], v[10:11], v[90:91]
	s_add_u32 s12, s12, s38
	v_mov_b32_e32 v57, v13
	v_mov_b32_e32 v12, v58
	v_mov_b32_e32 v13, v42
	v_mov_b32_e32 v42, v59
	v_mov_b32_e32 v58, v60
	v_mov_b32_e32 v59, v50
	v_mov_b32_e32 v50, v61
	v_pk_add_f32 v[50:51], v[58:59], v[50:51]
	s_addc_u32 s13, s13, s39
	v_pk_add_f32 v[8:9], v[246:247], v[50:51]
	s_cmpk_lt_i32 s7, 0x2000
	v_pk_mul_f32 v[50:51], v[8:9], v[8:9]
	s_nop 0
	v_mov_b32_e32 v212, v50
	v_mov_b32_e32 v82, v51
	v_pk_add_f32 v[2:3], v[212:213], v[82:83]
	s_nop 0
	v_pk_add_f32 v[50:51], v[22:23], v[2:3]
	v_pk_mul_f32 v[2:3], v[22:23], v[2:3]
	v_mov_b32_e32 v22, v11
	v_mov_b32_e32 v51, v3
	v_pk_add_f32 v[2:3], v[56:57], v[50:51]
	s_nop 0
	v_pk_add_f32 v[2:3], v[2:3], v[70:71]
	s_nop 0
	v_add_f32_e32 v2, v2, v3
	ds_bpermute_b32 v3, v73, v2
	s_waitcnt lgkmcnt(0)
; __device__ __forceinline__ float wave_sum(float v) {
; #pragma unroll
;     for (int o = 1; o < 64; o <<= 1) v += __shfl_xor(v, o);
;     return v;
; __global__ void __launch_bounds__(NWAVES * 64, 2) trunk_fwd(Args args) {
;     ...
;                     const float rstd = 1.0f / sqrtf(wave_sum(s) * (1.0f / D) + EPS);
;                     const f32x4* gr = (const f32x4*)args.in[I_NF] + lane; f32x4* orow = (f32x4*)(args.out + (size_t)m * D) + lane;
; #pragma unroll
;                     for (int jj = 0; jj < 8; ++jj) { const f32x4 gg = gr[64 * jj]; orow[64 * jj] = (f32x4){v[jj].x * rstd * gg.x, v[jj].y * rstd * gg.y, v[jj].z * rstd * gg.z, v[jj].w * rstd * gg.w}; }
	v_add_f32_e32 v2, v2, v3
	ds_bpermute_b32 v3, v75, v2
	s_waitcnt lgkmcnt(0)
	v_add_f32_e32 v2, v2, v3
	ds_bpermute_b32 v3, v108, v2
	s_waitcnt lgkmcnt(0)
	v_add_f32_e32 v2, v2, v3
	ds_bpermute_b32 v3, v109, v2
	s_waitcnt lgkmcnt(0)
	v_add_f32_e32 v2, v2, v3
	ds_bpermute_b32 v3, v110, v2
	s_waitcnt lgkmcnt(0)
	v_add_f32_e32 v2, v2, v3
	ds_bpermute_b32 v3, v111, v2
	s_waitcnt lgkmcnt(0)
	v_add_f32_e32 v2, v2, v3
	v_fmamk_f32 v2, v2, 0x3a000000, v226
	v_cmp_gt_f32_e32 vcc, s22, v2
	v_mul_f32_e32 v3, 0x4f800000, v2
	s_nop 0
	v_cndmask_b32_e32 v2, v2, v3, vcc
	v_sqrt_f32_e32 v3, v2
	s_nop 0
	v_add_u32_e32 v4, -1, v3
	v_fma_f32 v10, -v4, v3, v2
	v_cmp_ge_f32_e64 s[4:5], 0, v10
	v_add_u32_e32 v10, 1, v3
	s_nop 0
	v_cndmask_b32_e64 v4, v3, v4, s[4:5]
	v_fma_f32 v3, -v10, v3, v2
	v_cmp_lt_f32_e64 s[4:5], 0, v3
	s_nop 1
	v_cndmask_b32_e64 v3, v4, v10, s[4:5]
	v_mul_f32_e32 v4, 0x37800000, v3
	v_cndmask_b32_e32 v3, v3, v4, vcc
	v_cmp_class_f32_e32 vcc, v2, v225
	s_nop 1
	v_cndmask_b32_e32 v2, v3, v2, vcc
	v_div_scale_f32 v3, s[4:5], v2, v2, 1.0
	v_rcp_f32_e32 v4, v3
	s_nop 0
	v_fma_f32 v10, -v3, v4, 1.0
	v_fmac_f32_e32 v4, v10, v4
	v_div_scale_f32 v10, vcc, 1.0, v2, 1.0
	v_mul_f32_e32 v15, v10, v4
	v_fma_f32 v17, -v3, v15, v10
	v_fmac_f32_e32 v15, v17, v4
	v_fma_f32 v3, -v3, v15, v10
	v_div_fmas_f32 v3, v3, v4, v15
	v_div_fixup_f32 v10, v3, v2, 1.0
	v_pk_mul_f32 v[2:3], v[10:11], v[24:25] op_sel_hi:[0,1]
	v_pk_mul_f32 v[24:25], v[10:11], v[26:27] op_sel_hi:[0,1]
	v_pk_mul_f32 v[20:21], v[126:127], v[24:25]
	v_pk_mul_f32 v[18:19], v[124:125], v[2:3]
	global_store_dwordx4 v[76:77], v[18:21], off nt
	s_nop 1
	v_pk_mul_f32 v[2:3], v[10:11], v[54:55] op_sel_hi:[0,1]
	v_pk_mul_f32 v[24:25], v[10:11], v[52:53] op_sel_hi:[0,1]
	v_pk_mul_f32 v[6:7], v[10:11], v[244:245] op_sel_hi:[0,1]
	v_mov_b32_e32 v15, v184
	v_mov_b32_e32 v17, v185
	v_pk_mul_f32 v[14:15], v[10:11], v[14:15] op_sel_hi:[0,1]
	v_mov_b32_e32 v4, v81
	v_pk_mul_f32 v[4:5], v[10:11], v[4:5] op_sel_hi:[0,1]
	v_pk_mul_f32 v[18:19], v[128:129], v[24:25]
	v_pk_mul_f32 v[20:21], v[130:131], v[2:3]
	global_store_dwordx4 v[76:77], v[18:21], off offset:1024 nt
	s_nop 1
	v_pk_mul_f32 v[2:3], v[10:11], v[12:13] op_sel_hi:[0,1]
	v_pk_mul_f32 v[12:13], v[10:11], v[44:45] op_sel_hi:[0,1]
	v_pk_mul_f32 v[18:19], v[132:133], v[2:3]
	v_pk_mul_f32 v[2:3], v[10:11], v[42:43] op_sel_hi:[0,1]
	v_pk_mul_f32 v[20:21], v[134:135], v[2:3]
	global_store_dwordx4 v[76:77], v[18:21], off offset:2048 nt
	s_nop 1
	v_pk_mul_f32 v[2:3], v[10:11], v[46:47] op_sel_hi:[0,1]
	v_pk_mul_f32 v[18:19], v[136:137], v[12:13]
	v_pk_mul_f32 v[20:21], v[138:139], v[2:3]
	global_store_dwordx4 v[76:77], v[18:21], off offset:3072 nt
	s_nop 1
	v_pk_mul_f32 v[2:3], v[10:11], v[48:49] op_sel_hi:[0,1]
	v_add_co_u32_e32 v12, vcc, s20, v76
	v_pk_mul_f32 v[18:19], v[140:141], v[2:3]
	v_pk_mul_f32 v[2:3], v[10:11], v[78:79] op_sel_hi:[0,1]
	v_pk_mul_f32 v[20:21], v[142:143], v[2:3]
	v_addc_co_u32_e32 v13, vcc, 0, v77, vcc
	global_store_dwordx4 v[12:13], v[18:21], off nt
	s_nop 1
	v_pk_mul_f32 v[2:3], v[10:11], v[8:9] op_sel_hi:[0,1]
	v_pk_mul_f32 v[6:7], v[144:145], v[6:7]
	v_pk_mul_f32 v[8:9], v[146:147], v[2:3]
	global_store_dwordx4 v[12:13], v[6:9], off offset:1024 nt
	s_nop 1
	v_pk_mul_f32 v[2:3], v[10:11], v[16:17] op_sel_hi:[0,1]
	v_pk_mul_f32 v[6:7], v[148:149], v[14:15]
	v_pk_mul_f32 v[8:9], v[150:151], v[2:3]
	global_store_dwordx4 v[12:13], v[6:9], off offset:2048 nt
	s_nop 1
	v_pk_mul_f32 v[2:3], v[10:11], v[22:23] op_sel_hi:[0,1]
	v_pk_mul_f32 v[2:3], v[152:153], v[2:3]
	v_pk_mul_f32 v[4:5], v[154:155], v[4:5]
	global_store_dwordx4 v[12:13], v[2:5], off offset:3072 nt
	s_nop 1
	s_cbranch_scc1 .LBB0_1349
